# speedup vs baseline: 1.0030x; 1.0030x over previous
.Lrec_giveup:
	s_mov_b32 s45, 0
	s_branch .Lrec_wait
.Lrec_allin:
	s_cmp_eq_u32 s55, 1
	s_cbranch_scc1 .Lrec_wdone
	v_add_u32_e32 v197, v173, v188
	ds_write_b128 v197, v[198:201] offset:1024
	v_add_u32_e32 v197, v173, v189
	ds_write_b128 v197, v[202:205] offset:2048
	v_add_u32_e32 v197, v173, v190
	ds_write_b128 v197, v[212:215] offset:3072
	v_add_u32_e32 v197, v173, v194
	ds_write_b128 v197, v[216:219] offset:4096
	v_add_u32_e32 v197, v173, v191
	ds_write_b128 v197, v[220:223] offset:5120
	v_add_u32_e32 v197, v173, v192
	ds_write_b128 v197, v[224:227] offset:6144
	v_add_u32_e32 v197, v173, v193
	ds_write_b128 v197, v[228:231] offset:7168
.Lrec_wdone:
	s_cmp_lt_u32 s36, 23
	s_cbranch_scc0 .Lrec_nogx
	global_load_dwordx4 v[160:163], v[206:207], off

.Lrec_ld2:
	v_lshl_add_u32 v176, s36, 19, v168
	v_lshl_add_u64 v[10:11], v[176:177], 2, s[14:15]
	global_load_dwordx4 v[208:211], v[10:11], off nt
.Lrec_ldone:
	v_add_u32_e32 v173, v173, v187
	s_waitcnt lgkmcnt(0)
	s_barrier
	ds_read_b128 v[0:3], v173 offset:1024
	ds_read_b128 v[4:7], v173 offset:2048
	ds_read_b128 v[8:11], v173 offset:3072
	ds_read_b128 v[12:15], v173 offset:4096
	ds_read_b128 v[16:19], v173 offset:5120
	ds_read_b128 v[20:23], v173 offset:6144
	ds_read_b128 v[24:27], v173 offset:7168
	s_waitcnt lgkmcnt(6)
	v_pk_add_f32 v[234:235], v[234:235], v[2:3]
	v_pk_add_f32 v[232:233], v[232:233], v[0:1]
	s_waitcnt lgkmcnt(5)
	v_pk_add_f32 v[234:235], v[234:235], v[6:7]
	v_pk_add_f32 v[232:233], v[232:233], v[4:5]
	s_waitcnt lgkmcnt(4)
	v_pk_add_f32 v[234:235], v[234:235], v[10:11]
	v_pk_add_f32 v[232:233], v[232:233], v[8:9]
	s_waitcnt lgkmcnt(3)
	v_pk_add_f32 v[234:235], v[234:235], v[14:15]
	v_pk_add_f32 v[232:233], v[232:233], v[12:13]
	s_waitcnt lgkmcnt(2)
	v_pk_add_f32 v[234:235], v[234:235], v[18:19]
	v_pk_add_f32 v[232:233], v[232:233], v[16:17]
	s_waitcnt lgkmcnt(1)
	v_pk_add_f32 v[234:235], v[234:235], v[22:23]
	v_pk_add_f32 v[232:233], v[232:233], v[20:21]
	s_waitcnt lgkmcnt(0)
	v_pk_add_f32 v[18:19], v[234:235], v[26:27]
	v_pk_add_f32 v[16:17], v[232:233], v[24:25]
	v_mul_f32_e32 v16, 0xbfb8aa3b, v16
	v_exp_f32_e32 v20, v16
	v_add_f32_e32 v16, v18, v18
	v_mul_f32_e32 v16, 0x3fb8aa3b, v16
	v_mul_f32_e32 v17, 0xbfb8aa3b, v17
	v_exp_f32_e32 v18, v16
	v_exp_f32_e32 v17, v17
	v_add_f32_e32 v18, 1.0, v18
	v_add_f32_e32 v16, 1.0, v17
	v_add_f32_e32 v17, 1.0, v20
	v_rcp_f32_e32 v18, v18
	v_rcp_f32_e32 v16, v16
	v_rcp_f32_e32 v173, v17
	v_fma_f32 v17, v18, -2.0, 1.0
	v_pk_mul_f32 v[16:17], v[172:173], v[16:17]
	s_nop 0
	v_add_f32_e32 v172, v16, v17
	v_add_f32_e32 v17, v172, v172
	v_mul_f32_e32 v17, 0x3fb8aa3b, v17
	v_mul_f32_e32 v16, 0xbfb8aa3b, v19
	v_exp_f32_e32 v17, v17
	v_exp_f32_e32 v16, v16
	v_add_f32_e32 v17, 1.0, v17
	v_add_f32_e32 v16, 1.0, v16
	v_rcp_f32_e32 v17, v17
	v_rcp_f32_e32 v16, v16
	v_fma_f32 v17, v17, -2.0, 1.0
	v_fma_mixlo_f16 v16, v16, v17, 0
	ds_write_b16 v171, v16
	s_and_saveexec_b64 s[10:11], s[4:5]
	s_cbranch_execz .Lrec_pubdone
	ds_read_b64 v[16:17], v195
	s_and_b32 s12, s36, 1
	s_lshl_b32 s12, s12, 18
	v_mov_b32_e32 v18, s12
	v_mov_b32_e32 v19, 0
	v_lshl_add_u64 v[20:21], v[240:241], 0, v[18:19]
	v_add_u32_e32 v18, s41, v185
	v_lshlrev_b64 v[18:19], 11, v[18:19]
	v_lshl_add_u64 v[22:23], v[180:181], 0, v[18:19]
	s_bfe_u32 s12, s36, 0x10001
	s_mul_i32 s12, s12, 0x40004000
	s_and_b64 vcc, exec, s[6:7]
	s_cbranch_vccz .Lrec_pubfast
	s_waitcnt lgkmcnt(0)
	v_or_b32_e32 v18, s12, v16
	v_or_b32_e32 v19, s12, v17
	global_store_dwordx2 v[20:21], v[18:19], off sc1
	global_store_dwordx2 v[22:23], v[16:17], off
	s_branch .Lrec_pubdone
